# attention phase start: rel-pos bias table staged to LDS with all 4-5 loads per thread issued at once (one memory round trip instead of 2-3 serialized)
# baseline (speedup 1.0000x reference)
; #define GAS __attribute__((address_space(1)))
; #define LAS __attribute__((address_space(3)))
; __device__ __forceinline__ int lane_id() { return (int)__builtin_amdgcn_mbcnt_hi(~0u, __builtin_amdgcn_mbcnt_lo(~0u, 0u)); }
; __global__ void __launch_bounds__(NWAVES * 64, 2) hybrid_fwd(Args args) {
;     ...
;             LAS float* biasL = (LAS float*)(F.lds + RING_OFF + A_BIAS);
;             int tid2 = F.wave * 64 + lane_id(); asm volatile("" : "+v"(tid2));
;             for (int i = tid2; i < NH * 257; i += NWAVES * 64) biasL[i] = *(const GAS float*)(F.rel_bias + (size_t)l * NH * 257 + i) * LOG2E;
.LBB0_462:
	s_andn2_b64 vcc, exec, s[0:1]
	s_cbranch_vccnz .LBB0_628
	v_mov_b32_e32 v0, v212
	s_movk_i32 s0, 0x808
	s_nop 0
	v_cmp_gt_i32_e32 vcc, s0, v0
	s_and_saveexec_b64 s[0:1], vcc
	s_cbranch_execz .LBB0_476
	s_waitcnt lgkmcnt(0)
	v_readlane_b32 s4, v250, 36
	v_readlane_b32 s18, v252, 12
	v_readlane_b32 s19, v252, 13
	v_lshlrev_b32_e32 v1, 2, v0
	s_nop 3
	s_mul_i32 s96, s4, 0x808
	s_lshl_b64 s[4:5], s[96:97], 2
	s_add_u32 s8, s18, s4
	s_addc_u32 s9, s19, s5
	v_readlane_b32 s4, v250, 4
	v_add_u32_e32 v6, 0x1000, v1
	v_add_u32_e32 v7, 0x2000, v1
	global_load_dword v2, v1, s[8:9]
	global_load_dword v3, v1, s[8:9] offset:2048
	global_load_dword v4, v6, s[8:9]
	global_load_dword v5, v6, s[8:9] offset:2048
	v_cmp_gt_u32_e32 vcc, 8, v0
	s_and_saveexec_b64 s[2:3], vcc
	global_load_dword v8, v7, s[8:9]
	s_or_b64 exec, exec, s[2:3]
	v_add_u32_e32 v9, s4, v1
	s_mov_b32 s6, 0x3fb8aa3b
	s_waitcnt vmcnt(0)
	v_mul_f32_e32 v2, s6, v2
	v_mul_f32_e32 v3, s6, v3
	v_mul_f32_e32 v4, s6, v4
	v_mul_f32_e32 v5, s6, v5
	ds_write_b32 v9, v2
	ds_write_b32 v9, v3 offset:2048
	ds_write_b32 v9, v4 offset:4096
	ds_write_b32 v9, v5 offset:6144
	s_and_saveexec_b64 s[2:3], vcc
	v_mul_f32_e32 v8, s6, v8
	ds_write_b32 v9, v8 offset:8192
	s_or_b64 exec, exec, s[2:3]
